# stack3 + dilated pass 2: pass-1 partial output read back with 8 coalesced dwordx4 loads staged through LDS + 64 ds_read_u16 instead of 64 global_load_ushort
# speedup vs baseline: 1.0053x; 1.0053x over previous
; template <int PASS>
; __device__ __forceinline__ void attn_a_pass(LAS unsigned char* lds_all, const bf16* ZA, bf16* Oabc, float* ML, const float* rel_bias, int gw, int ngw, int xcd, int inx, int tid) {
;     ...
;             const float2 ml = *(const float2*)(MLb + (size_t)(RSTR * r32) * 16); m_reg = ml.x; l_reg = ml.y;
;             if (hf == 0) li_l[r32] = l_reg;
;             asm volatile("s_waitcnt lgkmcnt(0)" ::: "memory");
;             unsigned short ob[4][16];
; #pragma unroll
;             for (int r = 0; r < 16; ++r) {
;                 const char* rowp = (const char*)(Ob + (size_t)(RSTR * ((r & 3) + 8 * (r >> 2))) * 3072);
;                 const unsigned lo = (unsigned)((RSTR * 4 * hf * 3072 + r32) * 2);
; #pragma unroll
;                 for (int d = 0; d < 4; ++d) ob[d][r] = *(const unsigned short*)(rowp + lo + 64 * d); }
; #pragma unroll
;             for (int d = 0; d < 4; ++d)
;                 asm volatile("" : "+v"(ob[d][0]), "+v"(ob[d][1]), "+v"(ob[d][2]), "+v"(ob[d][3]), "+v"(ob[d][4]), "+v"(ob[d][5]), "+v"(ob[d][6]), "+v"(ob[d][7]), "+v"(ob[d][8]), "+v"(ob[d][9]), "+v"(ob[d][10]), "+v"(ob[d][11]), "+v"(ob[d][12]), "+v"(ob[d][13]), "+v"(ob[d][14]), "+v"(ob[d][15]) :: "memory");
.LBB0_1020:
	s_or_b64 exec, exec, s[18:19]
	s_mulk_i32 s17, 0x1800
	s_mul_hi_u32 s18, s16, 0x1800
	s_add_i32 s18, s18, s17
	s_mulk_i32 s16, 0x1800
	v_mul_lo_u32 v0, v68, s58
	s_add_u32 s16, s38, s16
	v_or_b32_e32 v0, v0, v195
	s_addc_u32 s17, s39, s18
	v_lshlrev_b32_e32 v0, 1, v0
	v_lshl_add_u64 v[2:3], s[16:17], 0, v[0:1]
	v_add_co_u32_e32 v4, vcc, s93, v2
	s_waitcnt lgkmcnt(0)
	s_mov_b32 s18, 0x48000
	s_nop 0
	v_addc_co_u32_e32 v5, vcc, 0, v3, vcc
	v_add_co_u32_e32 v6, vcc, s58, v2
	v_ashrrev_i32_e32 v197, 4, v194
	s_nop 0
	v_addc_co_u32_e32 v7, vcc, 0, v3, vcc
	v_lshrrev_b32_e32 v162, 4, v194
	v_mul_u32_u24_e32 v162, 0x18000, v162
	v_and_b32_e32 v163, 15, v194
	v_lshl_add_u32 v162, v163, 4, v162
	v_mov_b32_e32 v163, 0
	v_lshl_add_u64 v[162:163], s[16:17], 0, v[162:163]
	global_load_dwordx4 v[130:133], v[162:163], off
	s_mov_b32 s94, 0x60000
	v_add_co_u32_e64 v164, s[98:99], s94, v162
	s_nop 1
	v_addc_co_u32_e64 v165, s[98:99], 0, v163, s[98:99]
	global_load_dwordx4 v[134:137], v[164:165], off
	s_mov_b32 s94, 0xc0000
	v_add_co_u32_e64 v164, s[98:99], s94, v162
	s_nop 1
	v_addc_co_u32_e64 v165, s[98:99], 0, v163, s[98:99]
	global_load_dwordx4 v[138:141], v[164:165], off
	s_mov_b32 s94, 0x120000
	v_add_co_u32_e64 v164, s[98:99], s94, v162
	s_nop 1
	v_addc_co_u32_e64 v165, s[98:99], 0, v163, s[98:99]
	global_load_dwordx4 v[142:145], v[164:165], off
	s_mov_b32 s94, 0x180000
	v_add_co_u32_e64 v164, s[98:99], s94, v162
	s_nop 1
	v_addc_co_u32_e64 v165, s[98:99], 0, v163, s[98:99]
	global_load_dwordx4 v[146:149], v[164:165], off
	s_mov_b32 s94, 0x1e0000
	v_add_co_u32_e64 v164, s[98:99], s94, v162
	s_nop 1
	v_addc_co_u32_e64 v165, s[98:99], 0, v163, s[98:99]
	global_load_dwordx4 v[150:153], v[164:165], off
	s_mov_b32 s94, 0x240000
	v_add_co_u32_e64 v164, s[98:99], s94, v162
	s_nop 1
	v_addc_co_u32_e64 v165, s[98:99], 0, v163, s[98:99]
	global_load_dwordx4 v[154:157], v[164:165], off
	s_mov_b32 s94, 0x2a0000
	v_add_co_u32_e64 v164, s[98:99], s94, v162
	s_nop 1
	v_addc_co_u32_e64 v165, s[98:99], 0, v163, s[98:99]
	global_load_dwordx4 v[158:161], v[164:165], off
	v_lshlrev_b32_e32 v166, 4, v194
	v_add_u32_e32 v166, s29, v166
	v_lshrrev_b32_e32 v167, 5, v194
	v_lshlrev_b32_e32 v167, 10, v167
	v_and_b32_e32 v168, 31, v194
	v_lshl_add_u32 v167, v168, 1, v167
	v_add_u32_e32 v167, s29, v167
	s_waitcnt vmcnt(0)
	ds_write_b128 v166, v[130:133]
	ds_write_b128 v166, v[134:137] offset:1024
	ds_write_b128 v166, v[138:141] offset:2048
	ds_write_b128 v166, v[142:145] offset:3072
	ds_write_b128 v166, v[146:149] offset:4096
	ds_write_b128 v166, v[150:153] offset:5120
	ds_write_b128 v166, v[154:157] offset:6144
	ds_write_b128 v166, v[158:161] offset:7168
	ds_read_u16 v12, v167 offset:256
	ds_read_u16 v14, v167 offset:320
	ds_read_u16 v15, v167 offset:384
	ds_read_u16 v13, v167 offset:448
	ds_read_u16 v16, v167 offset:512
	ds_read_u16 v17, v167 offset:576
	ds_read_u16 v20, v167 offset:640
	ds_read_u16 v21, v167 offset:704
	v_add_co_u32_e32 v4, vcc, s18, v2
	s_mov_b32 s18, 0xc0000
	s_nop 0
	v_addc_co_u32_e32 v5, vcc, 0, v3, vcc
	v_add_co_u32_e32 v6, vcc, s18, v2
	s_mov_b32 s18, 0xd8000
	s_nop 0
	v_addc_co_u32_e32 v7, vcc, 0, v3, vcc
	ds_read_u16 v22, v167 offset:768
	ds_read_u16 v23, v167 offset:832
	ds_read_u16 v24, v167 offset:896
	ds_read_u16 v25, v167 offset:960
	ds_read_u16 v26, v167 offset:2048
	ds_read_u16 v27, v167 offset:2112
	ds_read_u16 v28, v167 offset:2176
	ds_read_u16 v29, v167 offset:2240
	v_add_co_u32_e32 v4, vcc, s18, v2
	s_mov_b32 s18, 0x108000
	s_nop 0
	v_addc_co_u32_e32 v5, vcc, 0, v3, vcc
	v_add_co_u32_e32 v6, vcc, s49, v2
	v_lshlrev_b32_e32 v74, 4, v68
	s_nop 0
	v_addc_co_u32_e32 v7, vcc, 0, v3, vcc
	ds_read_u16 v30, v167 offset:2304
	ds_read_u16 v31, v167 offset:2368
	ds_read_u16 v32, v167 offset:2432
	ds_read_u16 v33, v167 offset:2496
	ds_read_u16 v40, v167 offset:2560
	ds_read_u16 v41, v167 offset:2624
	ds_read_u16 v42, v167 offset:2688
	ds_read_u16 v43, v167 offset:2752
	v_add_co_u32_e32 v4, vcc, s18, v2
	s_mov_b32 s18, 0x180000
	s_nop 0
	v_addc_co_u32_e32 v5, vcc, 0, v3, vcc
	v_add_co_u32_e32 v6, vcc, s18, v2
	s_mov_b32 s18, 0x198000
	s_nop 0
	v_addc_co_u32_e32 v7, vcc, 0, v3, vcc
	ds_read_u16 v44, v167 offset:2816
	ds_read_u16 v45, v167 offset:2880
	ds_read_u16 v46, v167 offset:2944
	ds_read_u16 v47, v167 offset:3008
	ds_read_u16 v48, v167 offset:4096
	ds_read_u16 v49, v167 offset:4160
	ds_read_u16 v60, v167 offset:4224
	ds_read_u16 v58, v167 offset:4288
	v_add_co_u32_e32 v4, vcc, s18, v2
	s_mov_b32 s18, 0x1c8000
	s_nop 0
	v_addc_co_u32_e32 v5, vcc, 0, v3, vcc
	v_add_co_u32_e32 v6, vcc, s59, v2
	v_add_u32_e32 v200, s28, v74
	s_nop 0
	v_addc_co_u32_e32 v7, vcc, 0, v3, vcc
	ds_read_u16 v59, v167 offset:4352
	ds_read_u16 v61, v167 offset:4416
	ds_read_u16 v62, v167 offset:4480
	ds_read_u16 v63, v167 offset:4544
	ds_read_u16 v64, v167 offset:4608
	ds_read_u16 v65, v167 offset:4672
	ds_read_u16 v67, v167 offset:4736
	ds_read_u16 v70, v167 offset:4800
	v_add_co_u32_e32 v4, vcc, s18, v2
	s_mov_b32 s18, 0x258000
	s_nop 0
	v_addc_co_u32_e32 v5, vcc, 0, v3, vcc
	v_add_co_u32_e32 v6, vcc, s96, v2
	v_bitop3_b32 v8, v68, v194, 7 bitop3:0x78
	s_nop 0
	v_addc_co_u32_e32 v7, vcc, 0, v3, vcc
	ds_read_u16 v71, v167 offset:4864
	ds_read_u16 v75, v167 offset:4928
	ds_read_u16 v76, v167 offset:4992
	ds_read_u16 v77, v167 offset:5056
	ds_read_u16 v78, v167 offset:6144
	ds_read_u16 v79, v167 offset:6208
	ds_read_u16 v80, v167 offset:6272
	ds_read_u16 v81, v167 offset:6336
	v_add_co_u32_e32 v4, vcc, s18, v2
	s_mov_b32 s18, 0x288000
	s_nop 0
	v_addc_co_u32_e32 v5, vcc, 0, v3, vcc
	v_add_co_u32_e32 v6, vcc, s75, v2
	v_lshlrev_b32_e32 v202, 2, v68
	s_nop 0
	v_addc_co_u32_e32 v7, vcc, 0, v3, vcc
	v_add_co_u32_e32 v2, vcc, s18, v2
	ds_read_u16 v82, v167 offset:6400
	ds_read_u16 v83, v167 offset:6464
	ds_read_u16 v84, v167 offset:6528
	ds_read_u16 v85, v167 offset:6592
	ds_read_u16 v86, v167 offset:6656
	ds_read_u16 v87, v167 offset:6720
	ds_read_u16 v88, v167 offset:6784
	ds_read_u16 v89, v167 offset:6848
	v_addc_co_u32_e32 v3, vcc, 0, v3, vcc
	ds_read_u16 v18, v167 offset:0
	ds_read_u16 v19, v167 offset:64
	ds_read_u16 v36, v167 offset:128
	ds_read_u16 v34, v167 offset:192
	ds_read_u16 v90, v167 offset:6912
	ds_read_u16 v91, v167 offset:6976
	ds_read_u16 v92, v167 offset:7040
	ds_read_u16 v93, v167 offset:7104
	v_lshlrev_b32_e32 v3, 4, v194
	v_lshlrev_b32_e32 v2, 3, v194
	v_and_b32_e32 v3, 0xc0, v3
	v_lshlrev_b32_e32 v4, 1, v194
	v_and_or_b32 v3, v2, 24, v3
	v_and_b32_e32 v4, 32, v4
	v_and_b32_e32 v2, 0x100, v2
	v_or3_b32 v2, v3, v4, v2
	v_and_b32_e32 v3, 15, v194
	v_lshlrev_b32_e32 v66, 4, v3
	v_and_b32_e32 v3, 0xfffff0, v197
	v_lshlrev_b32_e32 v4, 1, v197
	v_and_or_b32 v3, v4, 8, v3
	v_lshrrev_b32_e32 v3, 1, v3
	v_bfe_u32 v5, v194, 2, 2
	v_lshrrev_b32_e32 v4, 1, v197
	v_or_b32_e32 v3, v3, v5
	v_and_b32_e32 v5, 3, v197
	s_waitcnt vmcnt(0)
; __device__ __forceinline__ int crow(int r, int hi) { return (r & 3) + 8 * (r >> 2) + 4 * hi; }
; template <int PASS>
; __device__ __forceinline__ void attn_a_pass(LAS unsigned char* lds_all, const bf16* ZA, bf16* Oabc, float* ML, const float* rel_bias, int gw, int ngw, int xcd, int inx, int tid) {
;     ...
; #pragma unroll
;             for (int r = 0; r < 16; ++r) { const float lr = li_l[crow(r, hf)];
; #pragma unroll
;                 for (int d = 0; d < 4; ++d) o[d][r] = __uint_as_float((unsigned)ob[d][r] << 16) * lr; }
	s_waitcnt lgkmcnt(0)
	v_and_or_b32 v4, v4, 4, v5
	v_lshlrev_b32_e32 v69, 6, v4
	v_lshlrev_b32_e32 v4, 8, v197
	v_and_b32_e32 v5, -16, v194
	v_xad_u32 v198, v66, v5, v4
	ds_read_b128 v[4:7], v200
	v_lshlrev_b32_e32 v0, 8, v195
	v_lshlrev_b32_e32 v73, 9, v3
	v_lshlrev_b32_e32 v3, 16, v13
	v_lshlrev_b32_e32 v13, 16, v12
	v_lshlrev_b32_e32 v12, 16, v18
	v_lshl_add_u32 v201, v8, 4, v0
	ds_read_b128 v[8:11], v200 offset:32
	s_waitcnt lgkmcnt(1)
	v_pk_mul_f32 v[50:51], v[4:5], v[12:13]
	v_lshlrev_b32_e32 v13, 16, v14
	v_lshlrev_b32_e32 v12, 16, v19
	v_add_u32_e32 v199, s29, v2
	v_lshlrev_b32_e32 v2, 16, v34
	v_pk_mul_f32 v[34:35], v[4:5], v[12:13]
	v_lshlrev_b32_e32 v13, 16, v15
	v_lshlrev_b32_e32 v12, 16, v36
	v_pk_mul_f32 v[18:19], v[4:5], v[12:13]
	v_lshlrev_b32_e32 v13, 16, v22
	v_lshlrev_b32_e32 v12, 16, v16
	v_pk_mul_f32 v[52:53], v[6:7], v[12:13]
	v_lshlrev_b32_e32 v13, 16, v23
	v_lshlrev_b32_e32 v12, 16, v17
	v_pk_mul_f32 v[36:37], v[6:7], v[12:13]
	v_lshlrev_b32_e32 v13, 16, v24
	v_lshlrev_b32_e32 v12, 16, v20
	v_pk_mul_f32 v[2:3], v[4:5], v[2:3]
	v_lshlrev_b32_e32 v4, 16, v21
	v_pk_mul_f32 v[20:21], v[6:7], v[12:13]
	v_lshlrev_b32_e32 v13, 16, v30
	v_lshlrev_b32_e32 v12, 16, v26
	s_waitcnt lgkmcnt(0)
	v_pk_mul_f32 v[54:55], v[8:9], v[12:13]
	v_lshlrev_b32_e32 v13, 16, v31
	v_lshlrev_b32_e32 v12, 16, v27
	v_pk_mul_f32 v[38:39], v[8:9], v[12:13]
	v_lshlrev_b32_e32 v13, 16, v32
	v_lshlrev_b32_e32 v12, 16, v28
	v_pk_mul_f32 v[22:23], v[8:9], v[12:13]
	v_lshlrev_b32_e32 v13, 16, v44
	v_lshlrev_b32_e32 v12, 16, v40
	v_pk_mul_f32 v[56:57], v[10:11], v[12:13]
	v_lshlrev_b32_e32 v13, 16, v45
	v_lshlrev_b32_e32 v12, 16, v41
	v_pk_mul_f32 v[40:41], v[10:11], v[12:13]
	ds_read_b128 v[12:15], v200 offset:64
	v_lshlrev_b32_e32 v5, 16, v25
	v_pk_mul_f32 v[4:5], v[6:7], v[4:5]
	v_lshlrev_b32_e32 v7, 16, v33
	v_lshlrev_b32_e32 v6, 16, v29
	v_lshlrev_b32_e32 v17, 16, v46
	v_lshlrev_b32_e32 v16, 16, v42
	v_pk_mul_f32 v[6:7], v[8:9], v[6:7]
	v_lshlrev_b32_e32 v9, 16, v47
	v_lshlrev_b32_e32 v8, 16, v43
	v_pk_mul_f32 v[24:25], v[10:11], v[16:17]
	v_lshlrev_b32_e32 v17, 16, v59
	v_lshlrev_b32_e32 v16, 16, v48
	v_pk_mul_f32 v[8:9], v[10:11], v[8:9]
	v_lshlrev_b32_e32 v10, 16, v58
	ds_read_b128 v[30:33], v200 offset:96
	s_waitcnt lgkmcnt(1)
	v_pk_mul_f32 v[58:59], v[12:13], v[16:17]
	v_lshlrev_b32_e32 v17, 16, v61
	v_lshlrev_b32_e32 v16, 16, v49
	v_pk_mul_f32 v[42:43], v[12:13], v[16:17]
	v_lshlrev_b32_e32 v17, 16, v62
	v_lshlrev_b32_e32 v16, 16, v60
	v_pk_mul_f32 v[26:27], v[12:13], v[16:17]
	v_lshlrev_b32_e32 v17, 16, v71
	v_lshlrev_b32_e32 v16, 16, v64
	v_pk_mul_f32 v[60:61], v[14:15], v[16:17]
	v_lshlrev_b32_e32 v17, 16, v75
	v_lshlrev_b32_e32 v16, 16, v65
	v_pk_mul_f32 v[44:45], v[14:15], v[16:17]
	v_lshlrev_b32_e32 v17, 16, v76
	v_lshlrev_b32_e32 v16, 16, v67
	v_lshlrev_b32_e32 v11, 16, v63
	v_pk_mul_f32 v[28:29], v[14:15], v[16:17]
	v_lshlrev_b32_e32 v17, 16, v82
	v_lshlrev_b32_e32 v16, 16, v78
	v_pk_mul_f32 v[10:11], v[12:13], v[10:11]
	v_lshlrev_b32_e32 v13, 16, v77
	v_lshlrev_b32_e32 v12, 16, v70
	s_waitcnt lgkmcnt(0)
	v_pk_mul_f32 v[62:63], v[30:31], v[16:17]
	v_lshlrev_b32_e32 v17, 16, v83
	v_lshlrev_b32_e32 v16, 16, v79
	v_pk_mul_f32 v[12:13], v[14:15], v[12:13]
	v_lshlrev_b32_e32 v15, 16, v85
	v_lshlrev_b32_e32 v14, 16, v81
	v_pk_mul_f32 v[46:47], v[30:31], v[16:17]
	v_lshlrev_b32_e32 v17, 16, v84
	v_lshlrev_b32_e32 v16, 16, v80
	v_lshlrev_b32_e32 v49, 16, v90
	v_lshlrev_b32_e32 v48, 16, v86
	v_pk_mul_f32 v[14:15], v[30:31], v[14:15]
	v_pk_mul_f32 v[30:31], v[30:31], v[16:17]
	v_lshlrev_b32_e32 v17, 16, v93
	v_lshlrev_b32_e32 v16, 16, v89
	v_pk_mul_f32 v[64:65], v[32:33], v[48:49]
	v_lshlrev_b32_e32 v49, 16, v91
	v_lshlrev_b32_e32 v48, 16, v87
	v_lshlrev_b32_e32 v71, 16, v92
	v_lshlrev_b32_e32 v70, 16, v88
	v_mov_b32_e32 v67, v1
	v_and_b32_e32 v72, 48, v66
	v_pk_mul_f32 v[16:17], v[32:33], v[16:17]
	v_pk_mul_f32 v[48:49], v[32:33], v[48:49]
	v_pk_mul_f32 v[32:33], v[32:33], v[70:71]
	v_lshl_add_u64 v[192:193], s[6:7], 0, v[66:67]
	v_add3_u32 v0, s29, v73, v69
	v_xor_b32_e32 v66, 64, v198
	v_xor_b32_e32 v67, 32, v201
	v_xor_b32_e32 v68, 64, v201
	v_xor_b32_e32 v69, 0x60, v201
	v_sub_u32_e32 v70, 0, v74
	s_mov_b32 s20, 1
	v_add_u32_e32 v203, 0x20814, v70
	v_add_u32_e32 v204, 0xffffff80, v202
	s_mov_b64 s[18:19], 0
	v_add_u32_e32 v205, s29, v67
	v_add_u32_e32 v206, s29, v68
	v_add_u32_e32 v207, s29, v69
	v_add_u32_e32 v208, s29, v66
	v_add_u32_e32 v209, v0, v72
